# v15 + static s_setprio 3 for the expert-weight copy waves in both router phases (router task waves stay at 0)
# speedup vs baseline: 1.0115x; 1.0115x over previous
; #define LAS __attribute__((address_space(3)))
; template <class T> __device__ __forceinline__ T* wsp(const Frame& F, size_t off) { return (T*)(F.ws + off); }
;     LAS float* scr = (LAS float*)(F.lds + RING_OFF + F.wave * 16384);
;     const int gw = (ncu ? (int)blockIdx.x - cu0 : F.vcu) * NWAVES + F.wave, NGW = (ncu ? ncu : F.G) * NWAVES;
;     bf16* UP = wsp<bf16>(F, WS_WEUP); bf16* DN = wsp<bf16>(F, WS_WEDN);
;     for (int it = it0 + gw; it < it1; it += NGW) {
;         const int e = it / 384, r = it % 384; const size_t eo = (size_t)(layer * 64 + e) * 1024 * 256;
;         if (r < 128) p0_transpose_item(inp(F, I_WGATE) + eo, 1024, 256, UP + (size_t)e * 512 * 1024, 3, scr, r, F.lane);
;         else if (r < 256) p0_transpose_item(inp(F, I_WUP) + eo, 1024, 256, UP + (size_t)e * 512 * 1024, 4, scr, r - 128, F.lane);
;         else p0_transpose_item(inp(F, I_WDOWN) + eo, 256, 1024, DN + (size_t)e * 1024 * 256, 5, scr, r - 256, F.lane, 16.f);
.Lcv0_entry:
	s_setprio 3
	s_cmpk_lg_i32 s67, 0x100
	s_cbranch_scc1 .Lcv0_end
	v_mov_b32_e32 v2, v0
	s_mul_i32 s4, s71, 5
	s_movk_i32 s2, 0x500
	v_readfirstlane_b32 s5, v2
	s_movk_i32 s3, 0x2000
	s_ashr_i32 s5, s5, 6
	s_cmpk_lt_i32 s5, 3
	s_cbranch_scc1 .Lcv0_end
	s_add_i32 s5, s5, s4
	s_addk_i32 s5, 0x23fd
	s_cmpk_gt_i32 s5, 0x5fff
	s_cbranch_scc1 .Lcv0_end
	s_add_u32 s9, s38, 0x4800000
	s_addc_u32 s18, s39, 0
	s_add_u32 s19, s38, 0x2800000
	v_and_b32_e32 v1, 56, v2
	v_lshlrev_b32_e32 v2, 2, v2
	s_addc_u32 s20, s39, 0
	v_and_b32_e32 v10, 28, v2
	s_lshl_b32 s21, s5, 6
	s_lshl_b32 s22, s2, 6
	s_lshl_b32 s23, s5, 5
	s_lshl_b32 s40, s2, 5
	s_lshl_b32 s41, s5, 3
	s_lshl_b32 s42, s2, 3
	s_lshl_b32 s43, s5, 1
	s_lshl_b32 s44, s2, 1
	s_add_i32 s45, 0, 0x202a8
	s_waitcnt lgkmcnt(1)
	v_mov_b32_e32 v7, 0
	s_movk_i32 s46, 0x1000
	s_movk_i32 s47, 0x4000
	s_movk_i32 s48, 0x6000
	s_movk_i32 s49, 0x7000
	s_mov_b32 s4, 0x41800000
	s_movk_i32 s50, 0x7fff
	s_mov_b32 s51, 0xffff0000
	s_mov_b64 s[10:11], 0x600
	s_add_i32 s52, 0, 0x202a0
	s_add_i32 s53, 0, 0x20298
	v_mov_b32_e32 v11, 1
	v_mov_b32_e32 v12, 0x400
	v_mov_b32_e32 v13, 0x7c
	s_branch .Lcv0_07

; #define LAS __attribute__((address_space(3)))
; template <class T> __device__ __forceinline__ T* wsp(const Frame& F, size_t off) { return (T*)(F.ws + off); }
;     LAS float* scr = (LAS float*)(F.lds + RING_OFF + F.wave * 16384);
;     const int gw = (ncu ? (int)blockIdx.x - cu0 : F.vcu) * NWAVES + F.wave, NGW = (ncu ? ncu : F.G) * NWAVES;
;     bf16* UP = wsp<bf16>(F, WS_WEUP); bf16* DN = wsp<bf16>(F, WS_WEDN);
;     for (int it = it0 + gw; it < it1; it += NGW) {
;         const int e = it / 384, r = it % 384; const size_t eo = (size_t)(layer * 64 + e) * 1024 * 256;
;         if (r < 128) p0_transpose_item(inp(F, I_WGATE) + eo, 1024, 256, UP + (size_t)e * 512 * 1024, 3, scr, r, F.lane);
;         else if (r < 256) p0_transpose_item(inp(F, I_WUP) + eo, 1024, 256, UP + (size_t)e * 512 * 1024, 4, scr, r - 128, F.lane);
;         else p0_transpose_item(inp(F, I_WDOWN) + eo, 256, 1024, DN + (size_t)e * 1024 * 256, 5, scr, r - 256, F.lane, 16.f);
.Lcv1_entry:
	s_setprio 3
	s_cmpk_lg_i32 s67, 0x100
	s_cbranch_scc1 .Lcv1_end
	v_mov_b32_e32 v2, v0
	s_mul_i32 s4, s71, 6
	s_movk_i32 s2, 0x600
	v_readfirstlane_b32 s5, v2
	s_movk_i32 s3, 0x2000
	s_ashr_i32 s5, s5, 6
	s_add_i32 s5, s5, s4
	s_addk_i32 s5, 0x1ffe
	s_cmpk_gt_i32 s5, 0x5fff
	s_cbranch_scc1 .Lcv1_end
	s_add_u32 s9, s38, 0x4800000
	s_addc_u32 s18, s39, 0
	s_add_u32 s19, s38, 0x2800000
	v_and_b32_e32 v1, 56, v2
	v_lshlrev_b32_e32 v2, 2, v2
	s_addc_u32 s20, s39, 0
	v_and_b32_e32 v10, 28, v2
	s_lshl_b32 s21, s5, 6
	s_lshl_b32 s22, s2, 6
	s_lshl_b32 s23, s5, 5
	s_lshl_b32 s40, s2, 5
	s_lshl_b32 s41, s5, 3
	s_lshl_b32 s42, s2, 3
	s_lshl_b32 s43, s5, 1
	s_lshl_b32 s44, s2, 1
	s_add_i32 s45, 0, 0x202a8
	s_waitcnt lgkmcnt(1)
	v_mov_b32_e32 v7, 0
	s_movk_i32 s46, 0x1000
	s_movk_i32 s47, 0x4000
	s_movk_i32 s48, 0x6000
	s_movk_i32 s49, 0x7000
	s_mov_b32 s4, 0x41800000
	s_movk_i32 s50, 0x7fff
	s_mov_b32 s51, 0xffff0000
	s_mov_b64 s[10:11], 0x600
	s_add_i32 s52, 0, 0x202a0
	s_add_i32 s53, 0, 0x20298
	v_mov_b32_e32 v11, 1
	v_mov_b32_e32 v12, 0x400
	v_mov_b32_e32 v13, 0x7c
	s_branch .Lcv1_07
